# v32
# speedup vs baseline: 1.0079x; 1.0079x over previous
.LBB0_10:
	s_or_b64 exec, exec, s[16:17]
	s_mov_b32 s3, 0x124f80
	v_cmp_gt_i32_e32 vcc, s3, v18
	s_waitcnt lgkmcnt(0)
	s_and_saveexec_b64 s[10:11], vcc
	s_cbranch_execz .LBB0_20
	v_mbcnt_lo_u32_b32 v1, -1, 0
	v_mbcnt_hi_u32_b32 v2, -1, v1
	v_and_b32_e32 v3, 64, v2
	v_xor_b32_e32 v1, 1, v2
	v_add_u32_e32 v3, 64, v3
	v_cmp_lt_i32_e32 vcc, v1, v3
	v_xor_b32_e32 v4, 2, v2
	s_lshl_b32 s24, s18, 11
	v_cndmask_b32_e32 v1, v2, v1, vcc
	v_cmp_lt_i32_e32 vcc, v4, v3
	s_add_i32 s14, s24, 0xfff80000
	v_ashrrev_i32_e32 v19, 31, v18
	v_cndmask_b32_e32 v4, v2, v4, vcc
	v_lshlrev_b32_e32 v24, 2, v4
	v_xor_b32_e32 v4, 4, v2
	v_cmp_lt_i32_e32 vcc, v4, v3
	s_lshl_b32 s25, s18, 12
	s_ashr_i32 s15, s14, 31
	v_cndmask_b32_e32 v4, v2, v4, vcc
	v_lshlrev_b32_e32 v25, 2, v4
	v_xor_b32_e32 v4, 8, v2
	v_cmp_lt_i32_e32 vcc, v4, v3
	v_lshlrev_b32_e32 v1, 2, v1
	s_add_i32 s24, s24, 0xfff00000
	v_cndmask_b32_e32 v2, v2, v4, vcc
	v_lshlrev_b32_e32 v26, 2, v2
	v_and_b32_e32 v2, 15, v0
	v_cmp_eq_u32_e64 s[6:7], 0, v2
	v_lshlrev_b32_e32 v2, 1, v0
	v_lshl_or_b32 v27, s2, 11, v2
	v_lshl_add_u64 v[2:3], v[18:19], 3, s[8:9]
	s_add_i32 s25, s25, 0xfff00000
	v_lshl_add_u64 v[20:21], v[2:3], 0, 4
	s_lshl_b64 s[16:17], s[14:15], 3
	s_lshl_b32 s15, s18, 10
	s_mov_b64 s[18:19], 0
	s_mov_b32 s26, 0x42fe0000
	s_movk_i32 s27, 0xff
	s_mov_b32 s28, 0x124f7f
	s_branch .LBB0_13

_Z3k_BPKiS0_PiS1_PKfPDF16_:
	v_cmp_eq_u32_e32 vcc, 0, v0
	s_and_saveexec_b64 s[4:5], vcc
	v_mov_b32_e32 v2, 0
	v_mov_b32_e32 v3, v2
	ds_write_b64 v2, v[2:3] offset:27712
	s_or_b64 exec, exec, s[4:5]
	s_load_dwordx2 s[24:25], s[0:1], 0x0
	s_load_dwordx4 s[36:39], s[0:1], 0x20
	s_movk_i32 s3, 0x100
	v_cmp_gt_u32_e32 vcc, s3, v0
	v_mbcnt_lo_u32_b32 v16, -1, 0
	v_and_b32_e32 v14, 63, v0
	s_waitcnt lgkmcnt(0)
	s_barrier
	s_lshl_b32 s40, s2, 10
	s_add_i32 s40, s40, 0x124f80
	v_add_u32_e32 v60, s40, v0
	v_min_u32_e32 v61, 0x1869ff, v60
	v_lshlrev_b32_e32 v61, 5, v61
	global_load_dwordx4 v[28:31], v61, s[36:37]
	global_load_dwordx4 v[32:35], v61, s[36:37] offset:16
	s_and_saveexec_b64 s[6:7], vcc
	s_cbranch_execz .LBB1_12
	s_load_dwordx2 s[4:5], s[0:1], 0x8
	s_lshl_b32 s3, s2, 8
	v_or_b32_e32 v2, s3, v0
	s_addk_i32 s3, 0x100
	v_ashrrev_i32_e32 v3, 31, v2
	v_or_b32_e32 v4, s3, v0
	s_waitcnt lgkmcnt(0)
	v_lshl_add_u64 v[2:3], v[2:3], 2, s[4:5]
	v_ashrrev_i32_e32 v5, 31, v4
	v_lshl_add_u64 v[4:5], v[4:5], 2, s[4:5]
	global_load_dword v1, v[2:3], off
	global_load_dword v6, v[4:5], off
	v_mbcnt_hi_u32_b32 v2, -1, v16
	v_and_b32_e32 v3, 64, v2
	v_xor_b32_e32 v4, 32, v2
	v_add_u32_e32 v3, 64, v3
	v_cmp_lt_i32_e64 s[4:5], v4, v3
	v_xor_b32_e32 v7, 16, v2
	v_xor_b32_e32 v8, 8, v2
	v_cndmask_b32_e64 v4, v2, v4, s[4:5]
	v_lshlrev_b32_e32 v4, 2, v4
	v_cmp_lt_i32_e64 s[4:5], v7, v3
	v_xor_b32_e32 v9, 4, v2
	v_xor_b32_e32 v10, 2, v2
	v_cndmask_b32_e64 v7, v2, v7, s[4:5]
	v_lshlrev_b32_e32 v7, 2, v7
	v_cmp_lt_i32_e64 s[4:5], v8, v3
	v_xor_b32_e32 v11, 1, v2
	s_movk_i32 s3, 0x1870
	v_cndmask_b32_e64 v8, v2, v8, s[4:5]
	v_lshlrev_b32_e32 v8, 2, v8
	v_cmp_lt_i32_e64 s[4:5], v9, v3
	v_lshlrev_b32_e32 v5, 2, v0
	s_waitcnt vmcnt(1)
	ds_bpermute_b32 v12, v4, v1
	s_waitcnt vmcnt(0)
	v_sub_u32_e32 v6, v6, v1
	ds_bpermute_b32 v4, v4, v6
	v_cndmask_b32_e64 v9, v2, v9, s[4:5]
	v_lshlrev_b32_e32 v9, 2, v9
	s_waitcnt lgkmcnt(1)
	v_add_u32_e32 v12, v12, v1
	ds_bpermute_b32 v13, v7, v12
	s_waitcnt lgkmcnt(1)
	v_add_u32_e32 v4, v4, v6
	ds_bpermute_b32 v7, v7, v4
	v_cmp_lt_i32_e64 s[4:5], v10, v3
	s_waitcnt lgkmcnt(1)
	v_add_u32_e32 v12, v13, v12
	v_cndmask_b32_e64 v10, v2, v10, s[4:5]
	s_waitcnt lgkmcnt(0)
	v_add_u32_e32 v4, v7, v4
	ds_bpermute_b32 v7, v8, v12
	ds_bpermute_b32 v8, v8, v4
	v_lshlrev_b32_e32 v10, 2, v10
	v_cmp_lt_i32_e64 s[4:5], v11, v3
	s_waitcnt lgkmcnt(1)
	v_add_u32_e32 v7, v7, v12
	s_waitcnt lgkmcnt(0)
	v_add_u32_e32 v4, v8, v4
	ds_bpermute_b32 v8, v9, v7
	ds_bpermute_b32 v9, v9, v4
	v_cndmask_b32_e64 v2, v2, v11, s[4:5]
	v_lshlrev_b32_e32 v2, 2, v2
	v_cmp_eq_u32_e64 s[4:5], 0, v14
	s_waitcnt lgkmcnt(1)
	v_add_u32_e32 v7, v8, v7
	s_waitcnt lgkmcnt(0)
	v_add_u32_e32 v4, v9, v4
	ds_bpermute_b32 v8, v10, v7
	ds_bpermute_b32 v9, v10, v4
	v_mad_u32_u24 v10, v0, s3, v1
	ds_write2st64_b32 v5, v6, v10 offset0:96 offset1:100
	v_mov_b32_e32 v6, 0
	s_waitcnt lgkmcnt(2)
	v_add_u32_e32 v3, v8, v7
	s_waitcnt lgkmcnt(1)
	v_add_u32_e32 v1, v9, v4
	ds_bpermute_b32 v4, v2, v3
	ds_bpermute_b32 v2, v2, v1
	ds_write_b32 v5, v6 offset:26624
	s_and_b64 exec, exec, s[4:5]
	s_cbranch_execz .LBB1_12
	s_mov_b64 s[4:5], exec
	s_waitcnt lgkmcnt(2)
	v_add_u32_e32 v3, v4, v3
	s_mov_b32 s8, 0

.LBB1_90:
	s_or_b64 exec, exec, s[2:3]
	v_mov_b32_e32 v2, 0
	s_waitcnt lgkmcnt(0)
	s_barrier
	s_waitcnt vmcnt(0)
	s_mov_b32 s41, 0x186a00
	v_cmp_gt_u32_e32 vcc, s41, v60
	s_and_saveexec_b64 s[42:43], vcc
	s_cbranch_execz .Lkb_cv_done
	v_max3_f32 v36, |v28|, 0, |v29|
	v_max3_f32 v36, v36, |v30|, |v31|
	v_max3_f32 v36, v36, |v32|, |v33|
	v_max3_f32 v36, v36, |v34|, |v35|
	s_nop 1
	v_max_f32_dpp v36, v36, v36 quad_perm:[1,0,3,2] row_mask:0xf bank_mask:0xf bound_ctrl:1
	s_nop 1
	v_max_f32_dpp v36, v36, v36 quad_perm:[2,3,0,1] row_mask:0xf bank_mask:0xf bound_ctrl:1
	s_nop 1
	v_max_f32_dpp v36, v36, v36 row_half_mirror row_mask:0xf bank_mask:0xf bound_ctrl:1
	s_nop 1
	v_max_f32_dpp v36, v36, v36 row_mirror row_mask:0xf bank_mask:0xf bound_ctrl:1
	s_mov_b32 s44, 0x42fe0000
	v_div_scale_f32 v37, s[46:47], v36, v36, s44
	v_rcp_f32_e32 v38, v37
	v_div_scale_f32 v39, vcc, s44, v36, s44
	v_fma_f32 v40, -v37, v38, 1.0
	v_fmac_f32_e32 v38, v40, v38
	v_mul_f32_e32 v40, v39, v38
	v_fma_f32 v41, -v37, v40, v39
	v_fmac_f32_e32 v40, v41, v38
	v_fma_f32 v37, -v37, v40, v39
	v_div_fmas_f32 v37, v37, v38, v40
	v_div_fixup_f32 v37, v37, v36, s44
	v_cmp_lt_f32_e32 vcc, 0, v36
	s_nop 1
	v_cndmask_b32_e32 v37, 0, v37, vcc
	v_mul_f32_e32 v28, v28, v37
	v_mul_f32_e32 v29, v29, v37
	v_mul_f32_e32 v30, v30, v37
	v_mul_f32_e32 v31, v31, v37
	v_mul_f32_e32 v32, v32, v37
	v_mul_f32_e32 v33, v33, v37
	v_mul_f32_e32 v34, v34, v37
	v_mul_f32_e32 v35, v35, v37
	v_rndne_f32_e32 v28, v28
	v_rndne_f32_e32 v29, v29
	v_rndne_f32_e32 v30, v30
	v_rndne_f32_e32 v31, v31
	v_rndne_f32_e32 v32, v32
	v_rndne_f32_e32 v33, v33
	v_rndne_f32_e32 v34, v34
	v_rndne_f32_e32 v35, v35
	v_add_f32_e32 v28, 0x43000000, v28
	v_add_f32_e32 v29, 0x43000000, v29
	v_add_f32_e32 v30, 0x43000000, v30
	v_add_f32_e32 v31, 0x43000000, v31
	v_add_f32_e32 v32, 0x43000000, v32
	v_add_f32_e32 v33, 0x43000000, v33
	v_add_f32_e32 v34, 0x43000000, v34
	v_add_f32_e32 v35, 0x43000000, v35
	v_cvt_pk_u8_f32 v46, v28, 0, 0
	v_cvt_pk_u8_f32 v47, v32, 0, 0
	v_cvt_pk_u8_f32 v46, v29, 1, v46
	v_cvt_pk_u8_f32 v47, v33, 1, v47
	v_cvt_pk_u8_f32 v46, v30, 2, v46
	v_cvt_pk_u8_f32 v47, v34, 2, v47
	v_cvt_pk_u8_f32 v46, v31, 3, v46
	v_cvt_pk_u8_f32 v47, v35, 3, v47
	s_add_u32 s48, s38, 0x30f4200
	s_addc_u32 s49, s39, 0
	v_lshlrev_b32_e32 v48, 3, v60
	global_store_dwordx2 v48, v[46:47], s[48:49]
	v_and_b32_e32 v49, 15, v60
	v_cmp_eq_u32_e32 vcc, 0, v49
	s_and_b64 exec, exec, vcc
	s_cbranch_execz .Lkb_cv_done
	v_mul_f32_e32 v50, 0x41010204, v36
	v_lshrrev_b32_e32 v51, 4, v60
	v_lshlrev_b32_e32 v51, 2, v51
	s_add_u32 s50, s38, 0x495e400
	s_addc_u32 s51, s39, 0
	global_store_dword v51, v50, s[50:51]
.Lkb_cv_done:
	s_mov_b64 exec, s[42:43]
	ds_read_b32 v14, v2 offset:27716
	s_movk_i32 s2, 0x1801
	s_waitcnt lgkmcnt(0)
	v_cmp_gt_i32_e32 vcc, s2, v14
	s_mov_b64 s[2:3], -1
	s_cbranch_vccnz .LBB1_132
	s_and_saveexec_b64 s[2:3], s[14:15]
	s_cbranch_execz .LBB1_93
	v_lshrrev_b32_e32 v2, 15, v15
	v_and_b32_e32 v2, 0x1fffc, v2
	v_mov_b32_e32 v3, 1
	ds_add_rtn_u32 v2, v2, v3 offset:26624
	v_and_b32_e32 v16, 0x1ffff, v15
	s_waitcnt lgkmcnt(0)
	v_ashrrev_i32_e32 v3, 31, v2
	v_lshl_add_u64 v[2:3], v[2:3], 2, s[22:23]
	global_store_dword v[2:3], v16, off

	.amdhsa_kernel _Z3k_BPKiS0_PiS1_PKfPDF16_
		.amdhsa_group_segment_fixed_size 27720
		.amdhsa_private_segment_fixed_size 0
		.amdhsa_kernarg_size 48
		.amdhsa_user_sgpr_count 2
		.amdhsa_user_sgpr_dispatch_ptr 0
		.amdhsa_user_sgpr_queue_ptr 0
		.amdhsa_user_sgpr_kernarg_segment_ptr 1
		.amdhsa_user_sgpr_dispatch_id 0
		.amdhsa_user_sgpr_kernarg_preload_length 0
		.amdhsa_user_sgpr_kernarg_preload_offset 0
		.amdhsa_user_sgpr_private_segment_size 0
		.amdhsa_uses_dynamic_stack 0
		.amdhsa_enable_private_segment 0
		.amdhsa_system_sgpr_workgroup_id_x 1
		.amdhsa_system_sgpr_workgroup_id_y 0
		.amdhsa_system_sgpr_workgroup_id_z 0
		.amdhsa_system_sgpr_workgroup_info 0
		.amdhsa_system_vgpr_workitem_id 0
		.amdhsa_next_free_vgpr 64
		.amdhsa_next_free_sgpr 52
		.amdhsa_accum_offset 64
		.amdhsa_reserve_vcc 1
		.amdhsa_float_round_mode_32 0
		.amdhsa_float_round_mode_16_64 0
		.amdhsa_float_denorm_mode_32 3
		.amdhsa_float_denorm_mode_16_64 3
		.amdhsa_dx10_clamp 1
		.amdhsa_ieee_mode 1
		.amdhsa_fp16_overflow 0
		.amdhsa_tg_split 0
		.amdhsa_exception_fp_ieee_invalid_op 0
		.amdhsa_exception_fp_denorm_src 0
		.amdhsa_exception_fp_ieee_div_zero 0
		.amdhsa_exception_fp_ieee_overflow 0
		.amdhsa_exception_fp_ieee_underflow 0
		.amdhsa_exception_fp_ieee_inexact 0
		.amdhsa_exception_int_div_zero 0
	.end_amdhsa_kernel

.Lfunc_end1:
	.size	_Z3k_BPKiS0_PiS1_PKfPDF16_, .Lfunc_end1-_Z3k_BPKiS0_PiS1_PKfPDF16_
	.set _Z3k_BPKiS0_PiS1_PKfPDF16_.num_vgpr, 64
	.set _Z3k_BPKiS0_PiS1_PKfPDF16_.num_agpr, 0
	.set _Z3k_BPKiS0_PiS1_PKfPDF16_.numbered_sgpr, 52
	.set _Z3k_BPKiS0_PiS1_PKfPDF16_.num_named_barrier, 0
	.set _Z3k_BPKiS0_PiS1_PKfPDF16_.private_seg_size, 0
	.set _Z3k_BPKiS0_PiS1_PKfPDF16_.uses_vcc, 1
	.set _Z3k_BPKiS0_PiS1_PKfPDF16_.uses_flat_scratch, 0
	.set _Z3k_BPKiS0_PiS1_PKfPDF16_.has_dyn_sized_stack, 0
	.set _Z3k_BPKiS0_PiS1_PKfPDF16_.has_recursion, 0
	.set _Z3k_BPKiS0_PiS1_PKfPDF16_.has_indirect_call, 0

amdhsa.kernels:
  - .agpr_count:     0
    .args:
      - .actual_access:  read_only
        .address_space:  global
        .offset:         0
        .size:           8
        .value_kind:     global_buffer
      - .actual_access:  read_only
        .address_space:  global
        .offset:         8
        .size:           8
        .value_kind:     global_buffer
      - .actual_access:  read_only
        .address_space:  global
        .offset:         16
        .size:           8
        .value_kind:     global_buffer
      - .actual_access:  read_only
        .address_space:  global
        .offset:         24
        .size:           8
        .value_kind:     global_buffer
      - .actual_access:  read_only
        .address_space:  global
        .offset:         32
        .size:           8
        .value_kind:     global_buffer
      - .actual_access:  read_only
        .address_space:  global
        .offset:         40
        .size:           8
        .value_kind:     global_buffer
      - .actual_access:  read_only
        .address_space:  global
        .offset:         48
        .size:           8
        .value_kind:     global_buffer
      - .actual_access:  write_only
        .address_space:  global
        .offset:         56
        .size:           8
        .value_kind:     global_buffer
      - .actual_access:  write_only
        .address_space:  global
        .offset:         64
        .size:           8
        .value_kind:     global_buffer
      - .actual_access:  write_only
        .address_space:  global
        .offset:         72
        .size:           8
        .value_kind:     global_buffer
      - .actual_access:  write_only
        .address_space:  global
        .offset:         80
        .size:           8
        .value_kind:     global_buffer
      - .actual_access:  write_only
        .address_space:  global
        .offset:         88
        .size:           8
        .value_kind:     global_buffer
      - .actual_access:  write_only
        .address_space:  global
        .offset:         96
        .size:           8
        .value_kind:     global_buffer
      - .actual_access:  write_only
        .address_space:  global
        .offset:         104
        .size:           8
        .value_kind:     global_buffer
      - .actual_access:  write_only
        .address_space:  global
        .offset:         112
        .size:           8
        .value_kind:     global_buffer
      - .actual_access:  write_only
        .address_space:  global
        .offset:         120
        .size:           8
        .value_kind:     global_buffer
      - .actual_access:  write_only
        .address_space:  global
        .offset:         128
        .size:           8
        .value_kind:     global_buffer
      - .offset:         136
        .size:           4
        .value_kind:     hidden_block_count_x
      - .offset:         140
        .size:           4
        .value_kind:     hidden_block_count_y
      - .offset:         144
        .size:           4
        .value_kind:     hidden_block_count_z
      - .offset:         148
        .size:           2
        .value_kind:     hidden_group_size_x
      - .offset:         150
        .size:           2
        .value_kind:     hidden_group_size_y
      - .offset:         152
        .size:           2
        .value_kind:     hidden_group_size_z
      - .offset:         154
        .size:           2
        .value_kind:     hidden_remainder_x
      - .offset:         156
        .size:           2
        .value_kind:     hidden_remainder_y
      - .offset:         158
        .size:           2
        .value_kind:     hidden_remainder_z
      - .offset:         176
        .size:           8
        .value_kind:     hidden_global_offset_x
      - .offset:         184
        .size:           8
        .value_kind:     hidden_global_offset_y
      - .offset:         192
        .size:           8
        .value_kind:     hidden_global_offset_z
      - .offset:         200
        .size:           2
        .value_kind:     hidden_grid_dims
    .group_segment_fixed_size: 27136
    .kernarg_segment_align: 8
    .kernarg_segment_size: 392
    .language:       OpenCL C
    .language_version:
      - 2
      - 0
    .max_flat_workgroup_size: 1024
    .name:           _Z3k_APKfPKiS2_S0_S0_S0_S0_PDF16_S3_S3_S3_PiS4_PhS5_PfS6_
    .private_segment_fixed_size: 0
    .sgpr_count:     40
    .sgpr_spill_count: 0
    .symbol:         _Z3k_APKfPKiS2_S0_S0_S0_S0_PDF16_S3_S3_S3_PiS4_PhS5_PfS6_.kd
    .uniform_work_group_size: 1
    .uses_dynamic_stack: false
    .vgpr_count:     48
    .vgpr_spill_count: 0
    .wavefront_size: 64
  - .agpr_count:     0
    .args:
      - .actual_access:  read_only
        .address_space:  global
        .offset:         0
        .size:           8
        .value_kind:     global_buffer
      - .actual_access:  read_only
        .address_space:  global
        .offset:         8
        .size:           8
        .value_kind:     global_buffer
      - .actual_access:  write_only
        .address_space:  global
        .offset:         16
        .size:           8
        .value_kind:     global_buffer
      - .actual_access:  write_only
        .address_space:  global
        .offset:         24
        .size:           8
        .value_kind:     global_buffer
      - .actual_access:  read_only
        .address_space:  global
        .offset:         32
        .size:           8
        .value_kind:     global_buffer
      - .actual_access:  read_only
        .address_space:  global
        .offset:         40
        .size:           8
        .value_kind:     global_buffer
    .group_segment_fixed_size: 27720
    .kernarg_segment_align: 8
    .kernarg_segment_size: 48
    .language:       OpenCL C
    .language_version:
      - 2
      - 0
    .max_flat_workgroup_size: 1024
    .name:           _Z3k_BPKiS0_PiS1_PKfPDF16_
    .private_segment_fixed_size: 0
    .sgpr_count:     58
    .sgpr_spill_count: 0
    .symbol:         _Z3k_BPKiS0_PiS1_PKfPDF16_.kd
    .uniform_work_group_size: 1
    .uses_dynamic_stack: false
    .vgpr_count:     64
    .vgpr_spill_count: 0
    .wavefront_size: 64
  - .agpr_count:     0
    .args:
      - .actual_access:  read_only
        .address_space:  global
        .offset:         0
        .size:           8
        .value_kind:     global_buffer
      - .actual_access:  read_only
        .address_space:  global
        .offset:         8
        .size:           8
        .value_kind:     global_buffer
      - .actual_access:  read_only
        .address_space:  global
        .offset:         16
        .size:           8
        .value_kind:     global_buffer
      - .actual_access:  read_only
        .address_space:  global
        .offset:         24
        .size:           8
        .value_kind:     global_buffer
      - .actual_access:  read_only
        .address_space:  global
        .offset:         32
        .size:           8
        .value_kind:     global_buffer
      - .actual_access:  read_only
        .address_space:  global
        .offset:         40
        .size:           8
        .value_kind:     global_buffer
      - .actual_access:  read_only
        .address_space:  global
        .offset:         48
        .size:           8
        .value_kind:     global_buffer
      - .actual_access:  write_only
        .address_space:  global
        .offset:         56
        .size:           8
        .value_kind:     global_buffer
      - .actual_access:  write_only
        .address_space:  global
        .offset:         64
        .size:           8
        .value_kind:     global_buffer
      - .actual_access:  write_only
        .address_space:  global
        .offset:         72
        .size:           8
        .value_kind:     global_buffer
    .group_segment_fixed_size: 30720
    .kernarg_segment_align: 8
    .kernarg_segment_size: 80
    .language:       OpenCL C
    .language_version:
      - 2
      - 0
    .max_flat_workgroup_size: 256
    .name:           _Z7k_layerILb1EEvPKvPKhPKfPKiS7_PKDF16_S5_PvPhPf
    .private_segment_fixed_size: 0
    .sgpr_count:     36
    .sgpr_spill_count: 0
    .symbol:         _Z7k_layerILb1EEvPKvPKhPKfPKiS7_PKDF16_S5_PvPhPf.kd
    .uniform_work_group_size: 1
    .uses_dynamic_stack: false
    .vgpr_count:     94
    .vgpr_spill_count: 0
    .wavefront_size: 64
  - .agpr_count:     0
    .args:
      - .actual_access:  read_only
        .address_space:  global
        .offset:         0
        .size:           8
        .value_kind:     global_buffer
      - .actual_access:  read_only
        .address_space:  global
        .offset:         8
        .size:           8
        .value_kind:     global_buffer
      - .actual_access:  read_only
        .address_space:  global
        .offset:         16
        .size:           8
        .value_kind:     global_buffer
      - .actual_access:  read_only
        .address_space:  global
        .offset:         24
        .size:           8
        .value_kind:     global_buffer
      - .actual_access:  read_only
        .address_space:  global
        .offset:         32
        .size:           8
        .value_kind:     global_buffer
      - .actual_access:  read_only
        .address_space:  global
        .offset:         40
        .size:           8
        .value_kind:     global_buffer
      - .actual_access:  read_only
        .address_space:  global
        .offset:         48
        .size:           8
        .value_kind:     global_buffer
      - .actual_access:  write_only
        .address_space:  global
        .offset:         56
        .size:           8
        .value_kind:     global_buffer
      - .actual_access:  read_only
        .address_space:  global
        .offset:         64
        .size:           8
        .value_kind:     global_buffer
      - .actual_access:  read_only
        .address_space:  global
        .offset:         72
        .size:           8
        .value_kind:     global_buffer
    .group_segment_fixed_size: 30720
    .kernarg_segment_align: 8
    .kernarg_segment_size: 80
    .language:       OpenCL C
    .language_version:
      - 2
      - 0
    .max_flat_workgroup_size: 256
    .name:           _Z7k_layerILb0EEvPKvPKhPKfPKiS7_PKDF16_S5_PvPhPf
    .private_segment_fixed_size: 0
    .sgpr_count:     34
    .sgpr_spill_count: 0
    .symbol:         _Z7k_layerILb0EEvPKvPKhPKfPKiS7_PKDF16_S5_PvPhPf.kd
    .uniform_work_group_size: 1
    .uses_dynamic_stack: false
    .vgpr_count:     92
    .vgpr_spill_count: 0
    .wavefront_size: 64
